# K2 epilogue hist reads batched
# speedup vs baseline: 1.0598x; 1.0230x over previous
.LBB1_167:
	s_or_b64 exec, exec, s[0:1]
	v_mov_b32_e32 v41, 0x18500
	v_or_b32_e32 v36, v165, v166
	v_or_b32_e32 v37, v158, v166
	v_or_b32_e32 v38, v150, v166
	v_or_b32_e32 v39, v146, v166
	v_lshl_or_b32 v40, v164, 4, v166
	v_add_u32_e32 v40, 0x140, v40
	v_lshl_add_u32 v36, v36, 2, v41
	v_lshl_add_u32 v37, v37, 2, v41
	v_lshl_add_u32 v38, v38, 2, v41
	v_lshl_add_u32 v39, v39, 2, v41
	v_lshl_add_u32 v40, v40, 2, v41
	ds_read_b32 v36, v36
	ds_read_b32 v37, v37
	ds_read_b32 v38, v38
	ds_read_b32 v39, v39
	ds_read_b32 v40, v40
	v_or_b32_e32 v23, v165, v166
	v_lshlrev_b32_e32 v0, 3, v167
	v_mov_b32_e32 v1, 0
	v_add_u32_e32 v22, s30, v23
	s_mov_b32 s2, 0x186a0
	v_lshl_add_u64 v[0:1], s[28:29], 0, v[0:1]
	v_cmp_gt_i32_e32 vcc, s2, v22
	s_and_saveexec_b64 s[0:1], vcc
	s_cbranch_execz .LBB1_169
	v_mov_b32_e32 v24, 0x18500
	v_lshl_add_u32 v23, v23, 2, v24
	s_waitcnt lgkmcnt(0)
	v_mov_b32_e32 v23, v36
	v_cvt_f32_u32_e32 v23, v23
	v_max_f32_e32 v23, 1.0, v23
	v_rsq_f32_e32 v24, v23
	v_ashrrev_i32_e32 v23, 31, v22
	v_lshlrev_b64 v[22:23], 5, v[22:23]
	v_pk_mul_f32 v[2:3], v[2:3], v[24:25] op_sel_hi:[1,0]
	v_pk_mul_f32 v[4:5], v[4:5], v[24:25] op_sel_hi:[1,0]
	v_cvt_pk_bf16_f32 v2, v2, v3
	v_cvt_pk_bf16_f32 v3, v4, v5
	v_lshl_add_u64 v[4:5], v[0:1], 0, v[22:23]
	global_store_dwordx2 v[4:5], v[2:3], off
.LBB1_169:
	s_or_b64 exec, exec, s[0:1]
	v_or_b32_e32 v3, v158, v166
	v_add_u32_e32 v2, s30, v3
	v_cmp_gt_i32_e32 vcc, s2, v2
	s_and_saveexec_b64 s[0:1], vcc
	s_cbranch_execz .LBB1_171
	v_mov_b32_e32 v4, 0x18500
	v_lshl_add_u32 v3, v3, 2, v4
	s_waitcnt lgkmcnt(0)
	v_mov_b32_e32 v3, v37
	v_cvt_f32_u32_e32 v3, v3
	v_max_f32_e32 v3, 1.0, v3
	v_rsq_f32_e32 v4, v3
	v_ashrrev_i32_e32 v3, 31, v2
	v_lshlrev_b64 v[2:3], 5, v[2:3]
	v_lshl_add_u64 v[2:3], v[0:1], 0, v[2:3]
	v_pk_mul_f32 v[6:7], v[6:7], v[4:5] op_sel_hi:[1,0]
	v_pk_mul_f32 v[4:5], v[8:9], v[4:5] op_sel_hi:[1,0]
	v_cvt_pk_bf16_f32 v6, v6, v7
	v_cvt_pk_bf16_f32 v7, v4, v5
	global_store_dwordx2 v[2:3], v[6:7], off
.LBB1_171:
	s_or_b64 exec, exec, s[0:1]
	v_or_b32_e32 v3, v150, v166
	v_add_u32_e32 v2, s30, v3
	v_cmp_gt_i32_e32 vcc, s2, v2
	s_and_saveexec_b64 s[0:1], vcc
	s_cbranch_execz .LBB1_173
	v_mov_b32_e32 v4, 0x18500
	v_lshl_add_u32 v3, v3, 2, v4
	s_waitcnt lgkmcnt(0)
	v_mov_b32_e32 v3, v38
	v_cvt_f32_u32_e32 v3, v3
	v_max_f32_e32 v3, 1.0, v3
	v_rsq_f32_e32 v4, v3
	v_ashrrev_i32_e32 v3, 31, v2
	v_lshlrev_b64 v[2:3], 5, v[2:3]
	v_lshl_add_u64 v[2:3], v[0:1], 0, v[2:3]
	v_pk_mul_f32 v[6:7], v[10:11], v[4:5] op_sel_hi:[1,0]
	v_pk_mul_f32 v[4:5], v[12:13], v[4:5] op_sel_hi:[1,0]
	v_cvt_pk_bf16_f32 v6, v6, v7
	v_cvt_pk_bf16_f32 v7, v4, v5
	global_store_dwordx2 v[2:3], v[6:7], off
.LBB1_173:
	s_or_b64 exec, exec, s[0:1]
	v_or_b32_e32 v3, v146, v166
	v_add_u32_e32 v2, s30, v3
	v_cmp_gt_i32_e32 vcc, s2, v2
	s_and_saveexec_b64 s[0:1], vcc
	s_cbranch_execz .LBB1_175
	v_mov_b32_e32 v4, 0x18500
	v_lshl_add_u32 v3, v3, 2, v4
	s_waitcnt lgkmcnt(0)
	v_mov_b32_e32 v3, v39
	v_cvt_f32_u32_e32 v3, v3
	v_max_f32_e32 v3, 1.0, v3
	v_rsq_f32_e32 v4, v3
	v_ashrrev_i32_e32 v3, 31, v2
	v_lshlrev_b64 v[2:3], 5, v[2:3]
	v_lshl_add_u64 v[2:3], v[0:1], 0, v[2:3]
	v_pk_mul_f32 v[6:7], v[14:15], v[4:5] op_sel_hi:[1,0]
	v_pk_mul_f32 v[4:5], v[16:17], v[4:5] op_sel_hi:[1,0]
	v_cvt_pk_bf16_f32 v6, v6, v7
	v_cvt_pk_bf16_f32 v7, v4, v5
	global_store_dwordx2 v[2:3], v[6:7], off
.LBB1_175:
	s_or_b64 exec, exec, s[0:1]
	v_lshl_or_b32 v2, v164, 4, v166
	v_add_u32_e32 v3, 0x140, v2
	v_add_u32_e32 v2, s30, v3
	s_mov_b32 s0, 0x186a0
	v_cmp_gt_i32_e32 vcc, s0, v2
	s_and_saveexec_b64 s[0:1], vcc
	s_cbranch_execz .LBB1_177
	v_mov_b32_e32 v4, 0x18500
	v_lshl_add_u32 v3, v3, 2, v4
	s_waitcnt lgkmcnt(0)
	v_mov_b32_e32 v3, v40
	v_cvt_f32_u32_e32 v3, v3
	v_max_f32_e32 v3, 1.0, v3
	v_rsq_f32_e32 v4, v3
	v_ashrrev_i32_e32 v3, 31, v2
	v_lshlrev_b64 v[2:3], 5, v[2:3]
	v_lshl_add_u64 v[0:1], v[0:1], 0, v[2:3]
	v_pk_mul_f32 v[6:7], v[18:19], v[4:5] op_sel_hi:[1,0]
	v_pk_mul_f32 v[4:5], v[20:21], v[4:5] op_sel_hi:[1,0]
	v_cvt_pk_bf16_f32 v6, v6, v7
	v_cvt_pk_bf16_f32 v7, v4, v5
	global_store_dwordx2 v[0:1], v[6:7], off
